# variant: every 8th arriver of an XCD starts an early L2 write-back
# baseline (speedup 1.0000x reference)
.LBB0_148:
	s_lshl_b32 s0, s27, 8
	s_add_u32 s4, s16, s0
	s_addc_u32 s5, s17, 0
	v_mov_b32_e32 v2, 0x1000
	v_mov_b32_e32 v4, 1
	global_atomic_add v4, v2, v4, s[4:5] offset:1024 sc0
	buffer_inv sc1
	v_cvt_f32_u32_e32 v2, v3
	v_sub_u32_e32 v5, 0, v3
	v_rcp_iflag_f32_e32 v2, v2
	s_nop 0
	v_mul_f32_e32 v2, 0x4f7ffffe, v2
	v_cvt_u32_f32_e32 v2, v2
	v_mul_lo_u32 v5, v5, v2
	v_mul_hi_u32 v5, v2, v5
	v_add_u32_e32 v2, v2, v5
	s_waitcnt vmcnt(0)
	v_mul_hi_u32 v2, v4, v2
	v_mul_lo_u32 v5, v2, v3
	v_sub_u32_e32 v5, v4, v5
	v_add_u32_e32 v6, 1, v2
	v_cmp_ge_u32_e32 vcc, v5, v3
	v_add_u32_e32 v4, 1, v4
	s_nop 0
	v_cndmask_b32_e32 v2, v2, v6, vcc
	v_sub_u32_e32 v6, v5, v3
	v_cndmask_b32_e32 v5, v5, v6, vcc
	v_add_u32_e32 v6, 1, v2
	v_cmp_ge_u32_e32 vcc, v5, v3
	s_nop 1
	v_cndmask_b32_e32 v2, v2, v6, vcc
	v_mul_lo_u32 v5, v3, v2
	v_add_u32_e32 v3, v5, v3
	v_cmp_ne_u32_e32 vcc, v4, v3
	s_and_saveexec_b64 s[0:1], vcc
	s_xor_b64 s[0:1], exec, s[0:1]
	s_cbranch_execz .LBB0_162
	v_sub_u32_e32 v6, v4, v5
	v_add_u32_e32 v6, -1, v6
	v_and_b32_e32 v6, 7, v6
	v_cmp_eq_u32_e32 vcc, 0, v6
	s_nop 4
	s_cbranch_vccz .Lhelp_skip_0
	buffer_wbl2 sc1

.LBB0_257:
	v_readlane_b32 s0, v254, 57
	v_readlane_b32 s1, v254, 58
	v_cvt_f32_u32_e32 v1, v3
	v_sub_u32_e32 v5, 0, v3
	v_rcp_iflag_f32_e32 v1, v1
	s_nop 1
	global_atomic_add v4, v34, v235, s[0:1] sc0
	buffer_inv sc1
	v_mul_f32_e32 v1, 0x4f7ffffe, v1
	v_cvt_u32_f32_e32 v1, v1
	v_mul_lo_u32 v5, v5, v1
	v_mul_hi_u32 v5, v1, v5
	v_add_u32_e32 v1, v1, v5
	s_waitcnt vmcnt(0)
	v_mul_hi_u32 v1, v4, v1
	v_mul_lo_u32 v5, v1, v3
	v_sub_u32_e32 v5, v4, v5
	v_add_u32_e32 v6, 1, v1
	v_cmp_ge_u32_e32 vcc, v5, v3
	v_add_u32_e32 v4, 1, v4
	s_nop 0
	v_cndmask_b32_e32 v1, v1, v6, vcc
	v_sub_u32_e32 v6, v5, v3
	v_cndmask_b32_e32 v5, v5, v6, vcc
	v_add_u32_e32 v6, 1, v1
	v_cmp_ge_u32_e32 vcc, v5, v3
	s_nop 1
	v_cndmask_b32_e32 v1, v1, v6, vcc
	v_mul_lo_u32 v5, v3, v1
	v_add_u32_e32 v3, v5, v3
	v_cmp_ne_u32_e32 vcc, v4, v3
	s_and_saveexec_b64 s[0:1], vcc
	s_xor_b64 s[0:1], exec, s[0:1]
	s_cbranch_execz .LBB0_271
	v_sub_u32_e32 v6, v4, v5
	v_add_u32_e32 v6, -1, v6
	v_and_b32_e32 v6, 7, v6
	v_cmp_eq_u32_e32 vcc, 0, v6
	s_nop 4
	s_cbranch_vccz .Lhelp_skip_1
	buffer_wbl2 sc1
